# SSD scan: the 16 two-byte y stores per lane and step replaced by two 16-byte stores (32x32 bf16 block transposed through a private LDS tile); counted waits renumbered
# speedup vs baseline: 1.0102x; 1.0059x over previous
; __device__ __forceinline__ float shl_from(float v, int src_lane) { return __int_as_float(__builtin_amdgcn_ds_bpermute(src_lane << 2, __float_as_int(v))); }
; __device__ __forceinline__ void ssd_unit(const Frame& F, int layer, int unit) {
;     ...
;         if (wave == 7) {
;             const float d0 = rd0, d1 = rd1;
;             const float da0 = d0 * a_coef, da1 = d1 * a_coef; const float ps = da0 + da1;
;             float inc = ps; float c0v, c1v;
;             if (dir == 0) {
; #pragma unroll
;                 for (int o = 1; o < 64; o <<= 1) { const float t = shl_from(inc, lane2 - o); if (lane2 >= o) inc += t; }
;                 c0v = inc - da1; c1v = inc;
;             } else {
; #pragma unroll
;                 for (int o = 1; o < 64; o <<= 1) { const float t = shl_from(inc, lane2 + o); if (lane2 + o < 64) inc += t; }
;                 c0v = inc; c1v = inc - da0;
;             }
;             const float tot = shl_from(inc, dir ? 0 : 63);
;             acs[2 * lane2] = c0v; acs[2 * lane2 + 1] = c1v; dtv[2 * lane2] = d0; dtv[2 * lane2 + 1] = d1;
;             wrow[2 * lane2] = __expf(tot - c0v) * d0; wrow[2 * lane2 + 1] = __expf(tot - c1v) * d1;
;             erow[2 * lane2] = __expf(c0v); erow[2 * lane2 + 1] = __expf(c1v);
;             if (lane2 == 0) aendp[0] = __expf(tot);
;         }
.LBB0_665:
	v_cndmask_b32_e64 v16, 0, 1, s[74:75]
	v_mov_b32_e32 v24, v133
	v_mov_b32_e32 v20, v252
	v_cmp_ne_u32_e64 s[44:45], 1, v16
	s_andn2_b64 vcc, exec, s[74:75]
	s_cbranch_vccnz .LBB0_673
	s_waitcnt vmcnt(2)
	v_mul_f32_e64 v21, v123, -v144
	v_fma_f32 v23, v122, -v144, v21
	v_lshlrev_b32_e32 v22, 2, v20
	s_mov_b64 s[2:3], -1
	s_and_b64 vcc, exec, s[42:43]
	v_cmp_gt_i32_e64 s[46:47], 32, v20
	s_cbranch_vccnz .LBB0_668
	ds_bpermute_b32 v16, v22, v23 offset:4
	v_cmp_gt_i32_e32 vcc, 63, v20
	v_mul_f32_e64 v19, v122, -v144
	s_mov_b64 s[2:3], 0
	s_waitcnt lgkmcnt(0)
	v_add_f32_e32 v16, v23, v16
	v_cndmask_b32_e32 v16, v23, v16, vcc
	ds_bpermute_b32 v17, v22, v16 offset:8
	v_cmp_gt_i32_e32 vcc, 62, v20
	s_waitcnt lgkmcnt(0)
	v_add_f32_e32 v17, v16, v17
	v_cndmask_b32_e32 v16, v16, v17, vcc
	ds_bpermute_b32 v17, v22, v16 offset:16
	v_cmp_gt_i32_e32 vcc, 60, v20
	s_waitcnt lgkmcnt(0)
	v_add_f32_e32 v17, v16, v17
	v_cndmask_b32_e32 v16, v16, v17, vcc
	ds_bpermute_b32 v17, v22, v16 offset:32
	v_cmp_gt_i32_e32 vcc, 56, v20
	s_waitcnt lgkmcnt(0)
	v_add_f32_e32 v17, v16, v17
	v_cndmask_b32_e32 v16, v16, v17, vcc
	ds_bpermute_b32 v17, v22, v16 offset:64
	v_cmp_gt_i32_e32 vcc, 48, v20
	s_waitcnt lgkmcnt(0)
	v_add_f32_e32 v17, v16, v17
	v_cndmask_b32_e32 v16, v16, v17, vcc
	ds_bpermute_b32 v17, v22, v16 offset:128
	s_waitcnt lgkmcnt(0)
	v_add_f32_e32 v17, v16, v17
	v_cndmask_b32_e64 v18, v16, v17, s[46:47]
	v_sub_f32_e32 v19, v18, v19
	v_mov_b64_e32 v[16:17], v[18:19]

; #define LAS __attribute__((address_space(3)))
; __device__ __forceinline__ unsigned pk2(float lo, float hi) { f32x2_t v = {lo, hi}; bf16x2_t b = __builtin_convertvector(v, bf16x2_t); return __builtin_bit_cast(unsigned, b); }
; __device__ __forceinline__ float bflo(unsigned w) { return __uint_as_float(w << 16); }
; __device__ __forceinline__ float bfhi(unsigned w) { return __uint_as_float(w & 0xffff0000u); }
; __device__ __forceinline__ void lds_barrier() { asm volatile("s_waitcnt lgkmcnt(0)" ::: "memory"); __builtin_amdgcn_s_barrier(); asm volatile("" ::: "memory"); }
; __device__ __forceinline__ void ssd_unit(const Frame& F, int layer, int unit) {
;     ...
;         lds_barrier();
;         {
;             u32x4 vg[4], vb[4]; float alr[4], wr_[4]; f32x4 ac0[4], ac1[4], dq0[4], dq1[4];
; #pragma unroll
;             for (int i = 0; i < 4; ++i) { const int idx = tid2 + 512 * i, r = idx >> 4, ch = idx & 15, s0 = ch * 8;
;                 vg[i] = *(LAS const u32x4*)(L + SS_GM + r * 272 + ch * 16); vb[i] = *(LAS const u32x4*)(L + SS_BM + r * 272 + ch * 16);
;                 alr[i] = acs[r]; wr_[i] = wrow[r];
;                 ac0[i] = *(LAS const f32x4*)(acs + s0); ac1[i] = *(LAS const f32x4*)(acs + s0 + 4); dq0[i] = *(LAS const f32x4*)(dtv + s0); dq1[i] = *(LAS const f32x4*)(dtv + s0 + 4); }
; #pragma unroll
;             for (int i = 0; i < 4; ++i) { const int idx = tid2 + 512 * i, r = idx >> 4, ch = idx & 15, s0 = ch * 8; float o[8];
; #pragma unroll
;                 for (int e = 0; e < 8; ++e) { const int s = s0 + e; const bool ok = dir ? (s >= r) : (s <= r);
;                     const float acv = (e < 4) ? ac0[i][e & 3] : ac1[i][e & 3], dtq = (e < 4) ? dq0[i][e & 3] : dq1[i][e & 3];
;                     const float gv = (e & 1) ? bfhi(vg[i][e >> 1]) : bflo(vg[i][e >> 1]); o[e] = ok ? gv * __expf(alr[i] - acv) * dtq : 0.f; }
;                 u32x4 w; w.x = pk2(o[0], o[1]); w.y = pk2(o[2], o[3]); w.z = pk2(o[4], o[5]); w.w = pk2(o[6], o[7]); *(LAS u32x4*)(L + SS_GM + r * 272 + ch * 16) = w;
;                 u32x4 wb;
; #pragma unroll
;                 for (int e = 0; e < 4; ++e) wb[e] = pk2(bflo(vb[i][e]) * wr_[i], bfhi(vb[i][e]) * wr_[i]);
;                 *(LAS u32x4*)(L + SS_BM + r * 272 + ch * 16) = wb; }
;         }
.LBB0_682:
	s_lshl_b32 s4, s80, 7
	v_and_b32_e32 v16, 15, v24
	s_cmpk_lt_i32 s80, 0x100
	v_lshlrev_b32_e32 v17, 4, v16
	v_ashrrev_i32_e32 v125, 4, v24
	s_cselect_b32 s5, s23, 0xffffff00
	s_cselect_b32 s6, s25, 0x80
	v_lshlrev_b32_e32 v197, 3, v16
	v_add_u32_e32 v25, s33, v17
	v_add_u32_e32 v26, 0, v17
	s_add_i32 s7, 0, 0x22400
	v_lshlrev_b32_e32 v16, 5, v16
	v_mul_lo_u32 v27, v125, s24
	v_add_u32_e32 v29, 0x200, v24
	v_add_u32_e32 v17, s7, v16
	v_add_u32_e32 v16, 0, v16
	v_add_u32_e32 v126, v25, v27
	v_add_u32_e32 v135, v26, v27
	v_lshlrev_b32_e32 v27, 2, v125
	s_add_i32 s10, 0, 0x22800
	v_ashrrev_i32_e32 v137, 4, v29
	s_waitcnt lgkmcnt(0)
	s_barrier
	v_add_u32_e32 v16, 0x22600, v16
	v_add_u32_e32 v28, s7, v27
	v_add_u32_e32 v27, s10, v27
	v_mul_lo_u32 v29, v137, s24
	ds_read_b128 v[36:39], v17
	ds_read_b128 v[20:23], v17 offset:16
	ds_read_b128 v[32:35], v16
	ds_read_b128 v[16:19], v16 offset:16
	ds_read_b128 v[210:213], v126
	ds_read_b128 v[214:217], v135 offset:18432
	v_add_u32_e32 v209, v25, v29
	ds_read_b32 v127, v28
	ds_read_b32 v124, v27
	ds_read_b128 v[108:111], v209
	v_lshlrev_b32_e32 v27, 2, v137
	v_add_u32_e32 v218, v26, v29
	v_add_u32_e32 v28, s7, v27
	v_add_u32_e32 v27, s10, v27
	ds_read_b128 v[104:107], v218 offset:18432
	ds_read_b32 v219, v28
	ds_read_b32 v136, v27
	v_add_u32_e32 v27, 0x400, v24
	v_add_u32_e32 v24, 0x600, v24
	v_ashrrev_i32_e32 v207, 4, v27
	v_ashrrev_i32_e32 v195, 4, v24
	v_mul_lo_u32 v27, v207, s24
	v_mul_lo_u32 v24, v195, s24
	s_waitcnt lgkmcnt(5)
	v_sub_f32_e32 v201, v127, v36
	v_add_u32_e32 v206, v25, v27
	v_add_u32_e32 v198, v26, v27
	v_lshlrev_b32_e32 v27, 2, v207
	v_add_u32_e32 v194, v25, v24
	v_add_u32_e32 v193, v26, v24
	v_lshlrev_b32_e32 v24, 2, v195
	v_mul_f32_e32 v201, 0x3fb8aa3b, v201
	v_add_u32_e32 v28, s7, v27
	v_add_u32_e32 v27, s10, v27
	v_add_u32_e32 v132, s7, v24
	v_add_u32_e32 v199, s10, v24
	v_cmp_le_i32_e32 vcc, v197, v125
	v_exp_f32_e32 v201, v201
	ds_read_b128 v[44:47], v206
	ds_read_b128 v[40:43], v198 offset:18432
	ds_read_b32 v208, v28
	ds_read_b32 v134, v27
	ds_read_b128 v[28:31], v194
	ds_read_b128 v[24:27], v193 offset:18432
	ds_read_b32 v196, v132
	ds_read_b32 v132, v199
	v_cndmask_b32_e64 v199, 0, 1, vcc
	v_cmp_ge_i32_e32 vcc, v197, v125
	v_sub_f32_e32 v202, v127, v37
	v_mul_f32_e32 v202, 0x3fb8aa3b, v202
	v_cndmask_b32_e64 v200, 0, 1, vcc
	v_cndmask_b32_e64 v199, v200, v199, s[40:41]
	v_lshlrev_b32_e32 v200, 16, v210
	v_and_b32_e32 v199, 1, v199
	v_mul_f32_e32 v200, v201, v200
	v_mul_f32_e32 v200, v32, v200
	v_cmp_eq_u32_e32 vcc, 1, v199
	v_or_b32_e32 v199, 1, v197
	v_exp_f32_e32 v202, v202
	v_cndmask_b32_e32 v220, 0, v200, vcc
	v_cmp_lt_i32_e32 vcc, v197, v125
	v_sub_f32_e32 v203, v127, v38
	v_mul_f32_e32 v203, 0x3fb8aa3b, v203
	v_cndmask_b32_e64 v200, 0, 1, vcc
	v_cmp_ge_i32_e32 vcc, v199, v125
	v_exp_f32_e32 v203, v203
	v_sub_f32_e32 v204, v127, v39
	v_cndmask_b32_e64 v201, 0, 1, vcc
	v_cndmask_b32_e64 v200, v201, v200, s[40:41]
	v_and_b32_e32 v201, 0xffff0000, v210
	v_and_b32_e32 v200, 1, v200
	v_mul_f32_e32 v201, v202, v201
	v_mul_f32_e32 v201, v33, v201
	v_cmp_eq_u32_e32 vcc, 1, v200
	v_or_b32_e32 v200, 2, v197
	v_mul_f32_e32 v204, 0x3fb8aa3b, v204
	v_cndmask_b32_e32 v210, 0, v201, vcc
	v_cmp_le_i32_e32 vcc, v200, v125
	v_exp_f32_e32 v204, v204
	v_sub_f32_e32 v205, v127, v20
	v_cndmask_b32_e64 v201, 0, 1, vcc
	v_cmp_ge_i32_e32 vcc, v200, v125
	v_mul_f32_e32 v205, 0x3fb8aa3b, v205
	v_exp_f32_e32 v205, v205
	v_cndmask_b32_e64 v202, 0, 1, vcc
	v_cndmask_b32_e64 v201, v202, v201, s[40:41]
	v_lshlrev_b32_e32 v202, 16, v211
	v_and_b32_e32 v201, 1, v201
	v_mul_f32_e32 v202, v203, v202
	v_mul_f32_e32 v202, v34, v202
	v_cmp_eq_u32_e32 vcc, 1, v201
	v_or_b32_e32 v201, 3, v197
	v_sub_f32_e32 v223, v127, v21
	v_cndmask_b32_e32 v221, 0, v202, vcc
	v_cmp_le_i32_e32 vcc, v201, v125
	v_mul_f32_e32 v223, 0x3fb8aa3b, v223
	v_exp_f32_e32 v223, v223
	v_cndmask_b32_e64 v202, 0, 1, vcc
	v_cmp_ge_i32_e32 vcc, v201, v125
	v_sub_f32_e32 v224, v127, v22
	v_mul_f32_e32 v224, 0x3fb8aa3b, v224
	v_cndmask_b32_e64 v203, 0, 1, vcc
	v_cndmask_b32_e64 v202, v203, v202, s[40:41]
	v_and_b32_e32 v203, 0xffff0000, v211
	v_and_b32_e32 v202, 1, v202
	v_mul_f32_e32 v203, v204, v203
	v_mul_f32_e32 v203, v35, v203
	v_cmp_eq_u32_e32 vcc, 1, v202
	v_or_b32_e32 v202, 4, v197
	v_exp_f32_e32 v224, v224
	v_cndmask_b32_e32 v211, 0, v203, vcc
	v_cmp_le_i32_e32 vcc, v202, v125
	v_sub_f32_e32 v127, v127, v23
	v_mul_f32_e32 v127, 0x3fb8aa3b, v127
	v_cndmask_b32_e64 v203, 0, 1, vcc
	v_cmp_ge_i32_e32 vcc, v202, v125
	v_exp_f32_e32 v127, v127
	v_cvt_pk_bf16_f32 v210, v220, v210
	v_cndmask_b32_e64 v204, 0, 1, vcc
	v_cndmask_b32_e64 v203, v204, v203, s[40:41]
	v_lshlrev_b32_e32 v204, 16, v212
	v_and_b32_e32 v203, 1, v203
	v_mul_f32_e32 v204, v205, v204
	v_mul_f32_e32 v204, v16, v204
	v_cmp_eq_u32_e32 vcc, 1, v203
	v_or_b32_e32 v203, 5, v197
	v_cvt_pk_bf16_f32 v211, v221, v211
	v_cndmask_b32_e32 v222, 0, v204, vcc
	v_cmp_le_i32_e32 vcc, v203, v125
	s_and_b32 s5, s5, s4
	s_and_b32 s4, s6, s4
	v_cndmask_b32_e64 v204, 0, 1, vcc
	v_cmp_ge_i32_e32 vcc, v203, v125
	s_add_i32 s4, s5, s4
	s_nop 0
	v_cndmask_b32_e64 v205, 0, 1, vcc
	v_cndmask_b32_e64 v204, v205, v204, s[40:41]
	v_and_b32_e32 v205, 0xffff0000, v212
	v_and_b32_e32 v204, 1, v204
	v_mul_f32_e32 v205, v223, v205
	v_mul_f32_e32 v205, v17, v205
	v_cmp_eq_u32_e32 vcc, 1, v204
	v_or_b32_e32 v204, 6, v197
	s_nop 0
	v_cndmask_b32_e32 v212, 0, v205, vcc
	v_cmp_le_i32_e32 vcc, v204, v125
	v_cvt_pk_bf16_f32 v212, v222, v212
	s_nop 0
	v_cndmask_b32_e64 v205, 0, 1, vcc
	v_cmp_ge_i32_e32 vcc, v204, v125
	s_nop 1
	v_cndmask_b32_e64 v223, 0, 1, vcc
	v_cndmask_b32_e64 v205, v223, v205, s[40:41]
	v_lshlrev_b32_e32 v223, 16, v213
	v_and_b32_e32 v205, 1, v205
	v_mul_f32_e32 v223, v224, v223
	v_mul_f32_e32 v223, v18, v223
	v_cmp_eq_u32_e32 vcc, 1, v205
	v_or_b32_e32 v205, 7, v197
	v_and_b32_e32 v213, 0xffff0000, v213
	v_cndmask_b32_e32 v223, 0, v223, vcc
	v_cmp_le_i32_e32 vcc, v205, v125
	v_mul_f32_e32 v127, v127, v213
	v_mul_f32_e32 v127, v19, v127
	v_cndmask_b32_e64 v224, 0, 1, vcc
	v_cmp_ge_i32_e32 vcc, v205, v125
	s_nop 1
	v_cndmask_b32_e64 v125, 0, 1, vcc
	v_cndmask_b32_e64 v125, v125, v224, s[40:41]
	v_and_b32_e32 v125, 1, v125
	v_cmp_eq_u32_e32 vcc, 1, v125
	s_nop 1
	v_cndmask_b32_e32 v125, 0, v127, vcc
	v_cvt_pk_bf16_f32 v213, v223, v125
	ds_write_b128 v126, v[210:213]
	v_lshlrev_b32_e32 v126, 16, v214
	v_and_b32_e32 v127, 0xffff0000, v214
	s_waitcnt lgkmcnt(13)
; #define LAS __attribute__((address_space(3)))
; __device__ __forceinline__ unsigned pk2(float lo, float hi) { f32x2_t v = {lo, hi}; bf16x2_t b = __builtin_convertvector(v, bf16x2_t); return __builtin_bit_cast(unsigned, b); }
; __device__ __forceinline__ float bflo(unsigned w) { return __uint_as_float(w << 16); }
; __device__ __forceinline__ float bfhi(unsigned w) { return __uint_as_float(w & 0xffff0000u); }
; __device__ __forceinline__ void lds_barrier() { asm volatile("s_waitcnt lgkmcnt(0)" ::: "memory"); __builtin_amdgcn_s_barrier(); asm volatile("" ::: "memory"); }
; __device__ __forceinline__ void ssd_unit(const Frame& F, int layer, int unit) {
;     ...
;         lds_barrier();
;         {
;             u32x4 vg[4], vb[4]; float alr[4], wr_[4]; f32x4 ac0[4], ac1[4], dq0[4], dq1[4];
; #pragma unroll
;             for (int i = 0; i < 4; ++i) { const int idx = tid2 + 512 * i, r = idx >> 4, ch = idx & 15, s0 = ch * 8;
;                 vg[i] = *(LAS const u32x4*)(L + SS_GM + r * 272 + ch * 16); vb[i] = *(LAS const u32x4*)(L + SS_BM + r * 272 + ch * 16);
;                 alr[i] = acs[r]; wr_[i] = wrow[r];
;                 ac0[i] = *(LAS const f32x4*)(acs + s0); ac1[i] = *(LAS const f32x4*)(acs + s0 + 4); dq0[i] = *(LAS const f32x4*)(dtv + s0); dq1[i] = *(LAS const f32x4*)(dtv + s0 + 4); }
; #pragma unroll
;             for (int i = 0; i < 4; ++i) { const int idx = tid2 + 512 * i, r = idx >> 4, ch = idx & 15, s0 = ch * 8; float o[8];
; #pragma unroll
;                 for (int e = 0; e < 8; ++e) { const int s = s0 + e; const bool ok = dir ? (s >= r) : (s <= r);
;                     const float acv = (e < 4) ? ac0[i][e & 3] : ac1[i][e & 3], dtq = (e < 4) ? dq0[i][e & 3] : dq1[i][e & 3];
;                     const float gv = (e & 1) ? bfhi(vg[i][e >> 1]) : bflo(vg[i][e >> 1]); o[e] = ok ? gv * __expf(alr[i] - acv) * dtq : 0.f; }
;                 u32x4 w; w.x = pk2(o[0], o[1]); w.y = pk2(o[2], o[3]); w.z = pk2(o[4], o[5]); w.w = pk2(o[6], o[7]); *(LAS u32x4*)(L + SS_GM + r * 272 + ch * 16) = w;
;                 u32x4 wb;
; #pragma unroll
;                 for (int e = 0; e < 4; ++e) wb[e] = pk2(bflo(vb[i][e]) * wr_[i], bfhi(vb[i][e]) * wr_[i]);
;                 *(LAS u32x4*)(L + SS_BM + r * 272 + ch * 16) = wb; }
;         }
	v_pk_mul_f32 v[126:127], v[124:125], v[126:127] op_sel_hi:[0,1]
	v_cvt_pk_bf16_f32 v210, v126, v127
	v_lshlrev_b32_e32 v126, 16, v215
	v_and_b32_e32 v127, 0xffff0000, v215
	v_pk_mul_f32 v[126:127], v[124:125], v[126:127] op_sel_hi:[0,1]
	v_cvt_pk_bf16_f32 v211, v126, v127
	v_lshlrev_b32_e32 v126, 16, v216
	v_and_b32_e32 v127, 0xffff0000, v216
	v_pk_mul_f32 v[126:127], v[124:125], v[126:127] op_sel_hi:[0,1]
	v_cvt_pk_bf16_f32 v212, v126, v127
	v_lshlrev_b32_e32 v126, 16, v217
	v_and_b32_e32 v127, 0xffff0000, v217
	v_pk_mul_f32 v[124:125], v[124:125], v[126:127] op_sel_hi:[0,1]
	s_waitcnt lgkmcnt(10)
	v_sub_f32_e32 v126, v219, v36
	v_mul_f32_e32 v126, 0x3fb8aa3b, v126
	v_cmp_le_i32_e32 vcc, v197, v137
	v_exp_f32_e32 v126, v126
	v_cvt_pk_bf16_f32 v213, v124, v125
	v_cndmask_b32_e64 v124, 0, 1, vcc
	v_cmp_ge_i32_e32 vcc, v197, v137
	v_sub_f32_e32 v127, v219, v37
	v_mul_f32_e32 v127, 0x3fb8aa3b, v127
	v_cndmask_b32_e64 v125, 0, 1, vcc
	v_cndmask_b32_e64 v124, v125, v124, s[40:41]
	v_lshlrev_b32_e32 v125, 16, v108
	v_and_b32_e32 v124, 1, v124
	v_mul_f32_e32 v125, v126, v125
	v_mul_f32_e32 v125, v32, v125
	v_cmp_eq_u32_e32 vcc, 1, v124
	v_exp_f32_e32 v127, v127
	v_and_b32_e32 v108, 0xffff0000, v108
	v_cndmask_b32_e32 v124, 0, v125, vcc
	v_cmp_lt_i32_e32 vcc, v197, v137
	v_mul_f32_e32 v108, v127, v108
	v_sub_f32_e32 v127, v219, v38
	v_cndmask_b32_e64 v125, 0, 1, vcc
	v_cmp_ge_i32_e32 vcc, v199, v137
	v_mul_f32_e32 v108, v33, v108
	v_mul_f32_e32 v127, 0x3fb8aa3b, v127
	v_cndmask_b32_e64 v126, 0, 1, vcc
	v_cndmask_b32_e64 v125, v126, v125, s[40:41]
	v_and_b32_e32 v125, 1, v125
	v_cmp_eq_u32_e32 vcc, 1, v125
	v_exp_f32_e32 v127, v127
	ds_write_b128 v135, v[210:213] offset:18432
	v_cndmask_b32_e32 v108, 0, v108, vcc
	v_cmp_le_i32_e32 vcc, v200, v137
	v_sub_f32_e32 v135, v219, v39
	v_mul_f32_e32 v135, 0x3fb8aa3b, v135
	v_cndmask_b32_e64 v125, 0, 1, vcc
	v_cmp_ge_i32_e32 vcc, v200, v137
	v_exp_f32_e32 v135, v135
	v_sub_f32_e32 v210, v219, v21
	v_cndmask_b32_e64 v126, 0, 1, vcc
	v_cndmask_b32_e64 v125, v126, v125, s[40:41]
	v_lshlrev_b32_e32 v126, 16, v109
	v_and_b32_e32 v125, 1, v125
	v_mul_f32_e32 v126, v127, v126
	v_mul_f32_e32 v126, v34, v126
	v_cmp_eq_u32_e32 vcc, 1, v125
	v_and_b32_e32 v109, 0xffff0000, v109
	v_mul_f32_e32 v109, v135, v109
	v_cndmask_b32_e32 v125, 0, v126, vcc
	v_cmp_le_i32_e32 vcc, v201, v137
	v_sub_f32_e32 v135, v219, v20
	v_mul_f32_e32 v109, v35, v109
	v_cndmask_b32_e64 v126, 0, 1, vcc
	v_cmp_ge_i32_e32 vcc, v201, v137
	v_mul_f32_e32 v135, 0x3fb8aa3b, v135
	v_exp_f32_e32 v135, v135
	v_cndmask_b32_e64 v127, 0, 1, vcc
	v_cndmask_b32_e64 v126, v127, v126, s[40:41]
	v_and_b32_e32 v126, 1, v126
	v_cmp_eq_u32_e32 vcc, 1, v126
	v_mul_f32_e32 v210, 0x3fb8aa3b, v210
	v_exp_f32_e32 v210, v210
	v_cndmask_b32_e32 v109, 0, v109, vcc
	v_cmp_le_i32_e32 vcc, v202, v137
	v_cvt_pk_bf16_f32 v108, v124, v108
	v_cvt_pk_bf16_f32 v109, v125, v109
	v_cndmask_b32_e64 v126, 0, 1, vcc
	v_cmp_ge_i32_e32 vcc, v202, v137
	s_nop 1
	v_cndmask_b32_e64 v127, 0, 1, vcc
	v_cndmask_b32_e64 v126, v127, v126, s[40:41]
	v_lshlrev_b32_e32 v127, 16, v110
	v_and_b32_e32 v126, 1, v126
	v_mul_f32_e32 v127, v135, v127
	v_mul_f32_e32 v127, v16, v127
	v_cmp_eq_u32_e32 vcc, 1, v126
	v_and_b32_e32 v110, 0xffff0000, v110
	v_mul_f32_e32 v110, v210, v110
	v_cndmask_b32_e32 v126, 0, v127, vcc
	v_cmp_le_i32_e32 vcc, v203, v137
	v_sub_f32_e32 v210, v219, v22
	v_mul_f32_e32 v110, v17, v110
	v_cndmask_b32_e64 v127, 0, 1, vcc
	v_cmp_ge_i32_e32 vcc, v203, v137
	v_mul_f32_e32 v210, 0x3fb8aa3b, v210
	v_exp_f32_e32 v210, v210
	v_cndmask_b32_e64 v135, 0, 1, vcc
	v_cndmask_b32_e64 v127, v135, v127, s[40:41]
	v_and_b32_e32 v127, 1, v127
	v_cmp_eq_u32_e32 vcc, 1, v127
	s_nop 1
	v_cndmask_b32_e32 v110, 0, v110, vcc
	v_cmp_le_i32_e32 vcc, v204, v137
	v_cvt_pk_bf16_f32 v110, v126, v110
	s_nop 0
	v_cndmask_b32_e64 v127, 0, 1, vcc
	v_cmp_ge_i32_e32 vcc, v204, v137
	s_nop 1
	v_cndmask_b32_e64 v135, 0, 1, vcc
	v_cndmask_b32_e64 v127, v135, v127, s[40:41]
	v_lshlrev_b32_e32 v135, 16, v111
	v_and_b32_e32 v127, 1, v127
	v_mul_f32_e32 v135, v210, v135
	v_sub_f32_e32 v210, v219, v23
	v_mul_f32_e32 v135, v18, v135
	v_cmp_eq_u32_e32 vcc, 1, v127
	v_mul_f32_e32 v210, 0x3fb8aa3b, v210
	v_exp_f32_e32 v210, v210
	v_cndmask_b32_e32 v127, 0, v135, vcc
	v_cmp_le_i32_e32 vcc, v205, v137
	v_and_b32_e32 v111, 0xffff0000, v111
	v_mul_f32_e32 v111, v210, v111
	v_cndmask_b32_e64 v135, 0, 1, vcc
	v_cmp_ge_i32_e32 vcc, v205, v137
	v_mul_f32_e32 v111, v19, v111
	s_nop 0
	v_cndmask_b32_e64 v137, 0, 1, vcc
	v_cndmask_b32_e64 v135, v137, v135, s[40:41]
	v_and_b32_e32 v135, 1, v135
	v_cmp_eq_u32_e32 vcc, 1, v135
	s_nop 1
	v_cndmask_b32_e32 v111, 0, v111, vcc
	v_cvt_pk_bf16_f32 v111, v127, v111
	ds_write_b128 v209, v[108:111]
	v_lshlrev_b32_e32 v108, 16, v104
	v_and_b32_e32 v109, 0xffff0000, v104
	s_waitcnt lgkmcnt(11)
	v_pk_mul_f32 v[108:109], v[136:137], v[108:109] op_sel_hi:[0,1]
	v_cvt_pk_bf16_f32 v104, v108, v109
	v_lshlrev_b32_e32 v108, 16, v105
	v_and_b32_e32 v109, 0xffff0000, v105
	v_pk_mul_f32 v[108:109], v[136:137], v[108:109] op_sel_hi:[0,1]
	v_cvt_pk_bf16_f32 v105, v108, v109
	v_lshlrev_b32_e32 v108, 16, v106
	v_and_b32_e32 v109, 0xffff0000, v106
	v_pk_mul_f32 v[108:109], v[136:137], v[108:109] op_sel_hi:[0,1]
	v_cvt_pk_bf16_f32 v106, v108, v109
	v_lshlrev_b32_e32 v108, 16, v107
	v_and_b32_e32 v109, 0xffff0000, v107
	v_pk_mul_f32 v[108:109], v[136:137], v[108:109] op_sel_hi:[0,1]
	v_cvt_pk_bf16_f32 v107, v108, v109
	ds_write_b128 v218, v[104:107] offset:18432
	s_waitcnt lgkmcnt(9)
; #define LAS __attribute__((address_space(3)))
; __device__ __forceinline__ unsigned pk2(float lo, float hi) { f32x2_t v = {lo, hi}; bf16x2_t b = __builtin_convertvector(v, bf16x2_t); return __builtin_bit_cast(unsigned, b); }
; __device__ __forceinline__ float bflo(unsigned w) { return __uint_as_float(w << 16); }
; __device__ __forceinline__ float bfhi(unsigned w) { return __uint_as_float(w & 0xffff0000u); }
; __device__ __forceinline__ void lds_barrier() { asm volatile("s_waitcnt lgkmcnt(0)" ::: "memory"); __builtin_amdgcn_s_barrier(); asm volatile("" ::: "memory"); }
; __device__ __forceinline__ void ssd_unit(const Frame& F, int layer, int unit) {
;     ...
;         lds_barrier();
;         {
;             u32x4 vg[4], vb[4]; float alr[4], wr_[4]; f32x4 ac0[4], ac1[4], dq0[4], dq1[4];
; #pragma unroll
;             for (int i = 0; i < 4; ++i) { const int idx = tid2 + 512 * i, r = idx >> 4, ch = idx & 15, s0 = ch * 8;
;                 vg[i] = *(LAS const u32x4*)(L + SS_GM + r * 272 + ch * 16); vb[i] = *(LAS const u32x4*)(L + SS_BM + r * 272 + ch * 16);
;                 alr[i] = acs[r]; wr_[i] = wrow[r];
;                 ac0[i] = *(LAS const f32x4*)(acs + s0); ac1[i] = *(LAS const f32x4*)(acs + s0 + 4); dq0[i] = *(LAS const f32x4*)(dtv + s0); dq1[i] = *(LAS const f32x4*)(dtv + s0 + 4); }
; #pragma unroll
;             for (int i = 0; i < 4; ++i) { const int idx = tid2 + 512 * i, r = idx >> 4, ch = idx & 15, s0 = ch * 8; float o[8];
; #pragma unroll
;                 for (int e = 0; e < 8; ++e) { const int s = s0 + e; const bool ok = dir ? (s >= r) : (s <= r);
;                     const float acv = (e < 4) ? ac0[i][e & 3] : ac1[i][e & 3], dtq = (e < 4) ? dq0[i][e & 3] : dq1[i][e & 3];
;                     const float gv = (e & 1) ? bfhi(vg[i][e >> 1]) : bflo(vg[i][e >> 1]); o[e] = ok ? gv * __expf(alr[i] - acv) * dtq : 0.f; }
;                 u32x4 w; w.x = pk2(o[0], o[1]); w.y = pk2(o[2], o[3]); w.z = pk2(o[4], o[5]); w.w = pk2(o[6], o[7]); *(LAS u32x4*)(L + SS_GM + r * 272 + ch * 16) = w;
;                 u32x4 wb;
; #pragma unroll
;                 for (int e = 0; e < 4; ++e) wb[e] = pk2(bflo(vb[i][e]) * wr_[i], bfhi(vb[i][e]) * wr_[i]);
;                 *(LAS u32x4*)(L + SS_BM + r * 272 + ch * 16) = wb; }
;         }
	v_sub_f32_e32 v106, v208, v36
	v_mul_f32_e32 v106, 0x3fb8aa3b, v106
	v_cmp_le_i32_e32 vcc, v197, v207
	v_exp_f32_e32 v106, v106
	v_sub_f32_e32 v107, v208, v37
	v_cndmask_b32_e64 v104, 0, 1, vcc
	v_cmp_ge_i32_e32 vcc, v197, v207
	v_mul_f32_e32 v107, 0x3fb8aa3b, v107
	v_exp_f32_e32 v107, v107
	v_cndmask_b32_e64 v105, 0, 1, vcc
	v_cndmask_b32_e64 v104, v105, v104, s[40:41]
	v_lshlrev_b32_e32 v105, 16, v44
	v_and_b32_e32 v104, 1, v104
	v_mul_f32_e32 v105, v106, v105
	v_mul_f32_e32 v105, v32, v105
	v_cmp_eq_u32_e32 vcc, 1, v104
	v_and_b32_e32 v44, 0xffff0000, v44
	v_mul_f32_e32 v44, v107, v44
	v_cndmask_b32_e32 v104, 0, v105, vcc
	v_cmp_lt_i32_e32 vcc, v197, v207
	v_sub_f32_e32 v107, v208, v38
	v_mul_f32_e32 v44, v33, v44
	v_cndmask_b32_e64 v105, 0, 1, vcc
	v_cmp_ge_i32_e32 vcc, v199, v207
	v_mul_f32_e32 v107, 0x3fb8aa3b, v107
	v_exp_f32_e32 v107, v107
	v_cndmask_b32_e64 v106, 0, 1, vcc
	v_cndmask_b32_e64 v105, v106, v105, s[40:41]
	v_and_b32_e32 v105, 1, v105
	v_cmp_eq_u32_e32 vcc, 1, v105
	v_sub_f32_e32 v108, v208, v39
	v_mul_f32_e32 v108, 0x3fb8aa3b, v108
	v_cndmask_b32_e32 v44, 0, v44, vcc
	v_cmp_le_i32_e32 vcc, v200, v207
	v_exp_f32_e32 v108, v108
	v_sub_f32_e32 v109, v208, v21
	v_cndmask_b32_e64 v105, 0, 1, vcc
	v_cmp_ge_i32_e32 vcc, v200, v207
	v_mul_f32_e32 v109, 0x3fb8aa3b, v109
	v_exp_f32_e32 v109, v109
	v_cndmask_b32_e64 v106, 0, 1, vcc
	v_cndmask_b32_e64 v105, v106, v105, s[40:41]
	v_lshlrev_b32_e32 v106, 16, v45
	v_and_b32_e32 v105, 1, v105
	v_mul_f32_e32 v106, v107, v106
	v_mul_f32_e32 v106, v34, v106
	v_cmp_eq_u32_e32 vcc, 1, v105
	v_and_b32_e32 v45, 0xffff0000, v45
	v_mul_f32_e32 v45, v108, v45
	v_cndmask_b32_e32 v105, 0, v106, vcc
	v_cmp_le_i32_e32 vcc, v201, v207
	v_sub_f32_e32 v108, v208, v20
	v_mul_f32_e32 v45, v35, v45
	v_cndmask_b32_e64 v106, 0, 1, vcc
	v_cmp_ge_i32_e32 vcc, v201, v207
	v_mul_f32_e32 v108, 0x3fb8aa3b, v108
	v_exp_f32_e32 v108, v108
	v_cndmask_b32_e64 v107, 0, 1, vcc
	v_cndmask_b32_e64 v106, v107, v106, s[40:41]
	v_and_b32_e32 v106, 1, v106
	v_cmp_eq_u32_e32 vcc, 1, v106
	v_sub_f32_e32 v110, v208, v23
	v_mul_f32_e32 v110, 0x3fb8aa3b, v110
	v_cndmask_b32_e32 v45, 0, v45, vcc
	v_cmp_le_i32_e32 vcc, v202, v207
	v_exp_f32_e32 v110, v110
	v_cvt_pk_bf16_f32 v44, v104, v44
	v_cndmask_b32_e64 v106, 0, 1, vcc
	v_cmp_ge_i32_e32 vcc, v202, v207
	v_cvt_pk_bf16_f32 v45, v105, v45
	s_waitcnt lgkmcnt(5)
	v_sub_f32_e32 v36, v196, v36
	v_cndmask_b32_e64 v107, 0, 1, vcc
	v_cndmask_b32_e64 v106, v107, v106, s[40:41]
	v_lshlrev_b32_e32 v107, 16, v46
	v_and_b32_e32 v106, 1, v106
	v_mul_f32_e32 v107, v108, v107
	v_mul_f32_e32 v107, v16, v107
	v_cmp_eq_u32_e32 vcc, 1, v106
	v_and_b32_e32 v46, 0xffff0000, v46
	v_mul_f32_e32 v46, v109, v46
	v_cndmask_b32_e32 v106, 0, v107, vcc
	v_cmp_le_i32_e32 vcc, v203, v207
	v_sub_f32_e32 v109, v208, v22
	v_mul_f32_e32 v46, v17, v46
	v_cndmask_b32_e64 v107, 0, 1, vcc
	v_cmp_ge_i32_e32 vcc, v203, v207
	v_mul_f32_e32 v109, 0x3fb8aa3b, v109
	v_exp_f32_e32 v109, v109
	v_cndmask_b32_e64 v108, 0, 1, vcc
	v_cndmask_b32_e64 v107, v108, v107, s[40:41]
	v_and_b32_e32 v107, 1, v107
	v_cmp_eq_u32_e32 vcc, 1, v107
	v_mul_f32_e32 v36, 0x3fb8aa3b, v36
	v_exp_f32_e32 v36, v36
	v_cndmask_b32_e32 v46, 0, v46, vcc
	v_cmp_le_i32_e32 vcc, v204, v207
	v_cvt_pk_bf16_f32 v46, v106, v46
	v_sub_f32_e32 v37, v196, v37
	v_cndmask_b32_e64 v107, 0, 1, vcc
	v_cmp_ge_i32_e32 vcc, v204, v207
	v_mul_f32_e32 v37, 0x3fb8aa3b, v37
	v_exp_f32_e32 v37, v37
	v_cndmask_b32_e64 v108, 0, 1, vcc
	v_cndmask_b32_e64 v107, v108, v107, s[40:41]
	v_lshlrev_b32_e32 v108, 16, v47
	v_and_b32_e32 v107, 1, v107
	v_mul_f32_e32 v108, v109, v108
	v_mul_f32_e32 v108, v18, v108
	v_cmp_eq_u32_e32 vcc, 1, v107
	v_and_b32_e32 v47, 0xffff0000, v47
	v_mul_f32_e32 v47, v110, v47
	v_cndmask_b32_e32 v107, 0, v108, vcc
	v_cmp_le_i32_e32 vcc, v205, v207
	v_mul_f32_e32 v47, v19, v47
	v_sub_f32_e32 v20, v196, v20
	v_cndmask_b32_e64 v108, 0, 1, vcc
	v_cmp_ge_i32_e32 vcc, v205, v207
	v_mul_f32_e32 v20, 0x3fb8aa3b, v20
	v_exp_f32_e32 v20, v20
	v_cndmask_b32_e64 v109, 0, 1, vcc
	v_cndmask_b32_e64 v108, v109, v108, s[40:41]
	v_and_b32_e32 v108, 1, v108
	v_cmp_eq_u32_e32 vcc, 1, v108
	v_sub_f32_e32 v21, v196, v21
	v_mul_f32_e32 v21, 0x3fb8aa3b, v21
	v_cndmask_b32_e32 v47, 0, v47, vcc
	v_cvt_pk_bf16_f32 v47, v107, v47
	ds_write_b128 v206, v[44:47]
	v_lshlrev_b32_e32 v44, 16, v40
	v_and_b32_e32 v45, 0xffff0000, v40
	v_pk_mul_f32 v[44:45], v[134:135], v[44:45] op_sel_hi:[0,1]
	v_cvt_pk_bf16_f32 v40, v44, v45
	v_lshlrev_b32_e32 v44, 16, v41
	v_and_b32_e32 v45, 0xffff0000, v41
	v_pk_mul_f32 v[44:45], v[134:135], v[44:45] op_sel_hi:[0,1]
	v_cvt_pk_bf16_f32 v41, v44, v45
	v_lshlrev_b32_e32 v44, 16, v42
	v_and_b32_e32 v45, 0xffff0000, v42
	v_pk_mul_f32 v[44:45], v[134:135], v[44:45] op_sel_hi:[0,1]
	v_cvt_pk_bf16_f32 v42, v44, v45
	v_lshlrev_b32_e32 v44, 16, v43
	v_and_b32_e32 v45, 0xffff0000, v43
	v_pk_mul_f32 v[44:45], v[134:135], v[44:45] op_sel_hi:[0,1]
	v_cvt_pk_bf16_f32 v43, v44, v45
	v_cmp_le_i32_e32 vcc, v197, v195
	ds_write_b128 v198, v[40:43] offset:18432
	v_exp_f32_e32 v21, v21
	v_cndmask_b32_e64 v40, 0, 1, vcc
	v_cmp_ge_i32_e32 vcc, v197, v195
	v_sub_f32_e32 v22, v196, v22
	v_mul_f32_e32 v22, 0x3fb8aa3b, v22
	v_cndmask_b32_e64 v41, 0, 1, vcc
	v_cndmask_b32_e64 v40, v41, v40, s[40:41]
	v_lshlrev_b32_e32 v41, 16, v28
	v_and_b32_e32 v40, 1, v40
	v_mul_f32_e32 v36, v36, v41
	v_mul_f32_e32 v32, v32, v36
	v_cmp_eq_u32_e32 vcc, 1, v40
	v_and_b32_e32 v28, 0xffff0000, v28
	v_mul_f32_e32 v28, v37, v28
	v_cndmask_b32_e32 v32, 0, v32, vcc
	v_cmp_lt_i32_e32 vcc, v197, v195
	v_sub_f32_e32 v37, v196, v38
	v_mul_f32_e32 v28, v33, v28
	v_cndmask_b32_e64 v36, 0, 1, vcc
; #define LAS __attribute__((address_space(3)))
; __device__ __forceinline__ unsigned pk2(float lo, float hi) { f32x2_t v = {lo, hi}; bf16x2_t b = __builtin_convertvector(v, bf16x2_t); return __builtin_bit_cast(unsigned, b); }
; __device__ __forceinline__ float bflo(unsigned w) { return __uint_as_float(w << 16); }
; __device__ __forceinline__ float bfhi(unsigned w) { return __uint_as_float(w & 0xffff0000u); }
; #define MFMA32(a, b, c) __builtin_amdgcn_mfma_f32_32x32x16_bf16((a), (b), (c), 0, 0, 0)
; __device__ __forceinline__ void ssd_unit(const Frame& F, int layer, int unit) {
;     ...
;             for (int i = 0; i < 4; ++i) { const int idx = tid2 + 512 * i, r = idx >> 4, ch = idx & 15, s0 = ch * 8; float o[8];
; #pragma unroll
;                 for (int e = 0; e < 8; ++e) { const int s = s0 + e; const bool ok = dir ? (s >= r) : (s <= r);
;                     const float acv = (e < 4) ? ac0[i][e & 3] : ac1[i][e & 3], dtq = (e < 4) ? dq0[i][e & 3] : dq1[i][e & 3];
;                     const float gv = (e & 1) ? bfhi(vg[i][e >> 1]) : bflo(vg[i][e >> 1]); o[e] = ok ? gv * __expf(alr[i] - acv) * dtq : 0.f; }
;                 u32x4 w; w.x = pk2(o[0], o[1]); w.y = pk2(o[2], o[3]); w.z = pk2(o[4], o[5]); w.w = pk2(o[6], o[7]); *(LAS u32x4*)(L + SS_GM + r * 272 + ch * 16) = w;
;                 u32x4 wb;
; #pragma unroll
;                 for (int e = 0; e < 4; ++e) wb[e] = pk2(bflo(vb[i][e]) * wr_[i], bfhi(vb[i][e]) * wr_[i]);
;                 *(LAS u32x4*)(L + SS_BM + r * 272 + ch * 16) = wb; }
;         }
;         lds_barrier();
;         {
;             const int lb = wave >> 1, pb = wave & 1; f32x16 y = {}, yo = {};
;             bf16x8 fa[8], fb[8];
; #pragma unroll
;             for (int ks = 0; ks < 8; ++ks) { fa[ks] = frag_rm(L + SS_GM, 272, 32 * lb, 16 * ks, lane); fb[ks] = frag_tr(L + SS_XS, SS_XS_STRIDE, 16 * ks, 32 * pb, lane); }
;             __builtin_amdgcn_sched_barrier(0);
; #pragma unroll
;             for (int ks = 0; ks < 8; ++ks) y = MFMA32(fa[ks], fb[ks], y);
; #pragma unroll
;             for (int ks = 0; ks < 8; ++ks) { fa[ks] = frag_rm(L + SS_CM, 272, 32 * lb, 16 * ks, lane); fb[ks] = frag_rm(L + SS_H, 272, 32 * pb, 16 * ks, lane); }
;             __builtin_amdgcn_sched_barrier(0);
; #pragma unroll
;             for (int ks = 0; ks < 8; ++ks) yo = MFMA32(fa[ks], fb[ks], yo);
	v_cmp_ge_i32_e32 vcc, v199, v195
	v_mul_f32_e32 v37, 0x3fb8aa3b, v37
	v_exp_f32_e32 v37, v37
	v_cndmask_b32_e64 v40, 0, 1, vcc
	v_cndmask_b32_e64 v36, v40, v36, s[40:41]
	v_and_b32_e32 v36, 1, v36
	v_cmp_eq_u32_e32 vcc, 1, v36
	v_exp_f32_e32 v22, v22
	s_nop 0
	v_cndmask_b32_e32 v28, 0, v28, vcc
	v_cmp_le_i32_e32 vcc, v200, v195
	s_nop 1
	v_cndmask_b32_e64 v33, 0, 1, vcc
	v_cmp_ge_i32_e32 vcc, v200, v195
	s_nop 1
	v_cndmask_b32_e64 v36, 0, 1, vcc
	v_cndmask_b32_e64 v33, v36, v33, s[40:41]
	v_lshlrev_b32_e32 v36, 16, v29
	v_and_b32_e32 v33, 1, v33
	v_mul_f32_e32 v36, v37, v36
	v_sub_f32_e32 v37, v196, v39
	v_mul_f32_e32 v34, v34, v36
	v_cmp_eq_u32_e32 vcc, 1, v33
	v_mul_f32_e32 v37, 0x3fb8aa3b, v37
	v_exp_f32_e32 v37, v37
	v_cndmask_b32_e32 v33, 0, v34, vcc
	v_cmp_le_i32_e32 vcc, v201, v195
	v_and_b32_e32 v29, 0xffff0000, v29
	v_mul_f32_e32 v29, v37, v29
	v_cndmask_b32_e64 v34, 0, 1, vcc
	v_cmp_ge_i32_e32 vcc, v201, v195
	v_mul_f32_e32 v29, v35, v29
	s_nop 0
	v_cndmask_b32_e64 v36, 0, 1, vcc
	v_cndmask_b32_e64 v34, v36, v34, s[40:41]
	v_and_b32_e32 v34, 1, v34
	v_cmp_eq_u32_e32 vcc, 1, v34
	s_nop 1
	v_cndmask_b32_e32 v29, 0, v29, vcc
	v_cmp_le_i32_e32 vcc, v202, v195
	s_nop 1
	v_cndmask_b32_e64 v34, 0, 1, vcc
	v_cmp_ge_i32_e32 vcc, v202, v195
	s_nop 1
	v_cndmask_b32_e64 v35, 0, 1, vcc
	v_cndmask_b32_e64 v34, v35, v34, s[40:41]
	v_lshlrev_b32_e32 v35, 16, v30
	v_and_b32_e32 v34, 1, v34
	v_mul_f32_e32 v20, v20, v35
	v_mul_f32_e32 v16, v16, v20
	v_cmp_eq_u32_e32 vcc, 1, v34
	v_and_b32_e32 v30, 0xffff0000, v30
	v_mul_f32_e32 v21, v21, v30
	v_cndmask_b32_e32 v20, 0, v16, vcc
	v_cmp_le_i32_e32 vcc, v203, v195
	v_mul_f32_e32 v17, v17, v21
	s_nop 0
	v_cndmask_b32_e64 v16, 0, 1, vcc
	v_cmp_ge_i32_e32 vcc, v203, v195
	s_nop 1
	v_cndmask_b32_e64 v34, 0, 1, vcc
	v_cndmask_b32_e64 v16, v34, v16, s[40:41]
	v_and_b32_e32 v16, 1, v16
	v_cmp_eq_u32_e32 vcc, 1, v16
	s_nop 1
	v_cndmask_b32_e32 v21, 0, v17, vcc
	v_cmp_le_i32_e32 vcc, v204, v195
	s_nop 1
	v_cndmask_b32_e64 v16, 0, 1, vcc
	v_cmp_ge_i32_e32 vcc, v204, v195
	s_nop 1
	v_cndmask_b32_e64 v17, 0, 1, vcc
	v_cndmask_b32_e64 v16, v17, v16, s[40:41]
	v_lshlrev_b32_e32 v17, 16, v31
	v_mul_f32_e32 v17, v22, v17
	v_and_b32_e32 v16, 1, v16
	v_mul_f32_e32 v17, v18, v17
	v_sub_f32_e32 v18, v196, v23
	v_cmp_eq_u32_e32 vcc, 1, v16
	v_mul_f32_e32 v18, 0x3fb8aa3b, v18
	v_exp_f32_e32 v18, v18
	v_cndmask_b32_e32 v22, 0, v17, vcc
	v_cmp_le_i32_e32 vcc, v205, v195
	s_nop 1
	v_cndmask_b32_e64 v16, 0, 1, vcc
	v_cmp_ge_i32_e32 vcc, v205, v195
	s_nop 1
	v_cndmask_b32_e64 v17, 0, 1, vcc
	v_cndmask_b32_e64 v16, v17, v16, s[40:41]
	v_and_b32_e32 v17, 0xffff0000, v31
	v_and_b32_e32 v16, 1, v16
	v_mul_f32_e32 v17, v18, v17
	v_mul_f32_e32 v17, v19, v17
	v_cmp_eq_u32_e32 vcc, 1, v16
	v_cvt_pk_bf16_f32 v16, v32, v28
	v_cvt_pk_bf16_f32 v18, v20, v21
	v_cndmask_b32_e32 v19, 0, v17, vcc
	v_cvt_pk_bf16_f32 v17, v33, v29
	v_cvt_pk_bf16_f32 v19, v22, v19
	ds_write_b128 v194, v[16:19]
	v_lshlrev_b32_e32 v16, 16, v24
	v_and_b32_e32 v17, 0xffff0000, v24
	v_lshlrev_b32_e32 v18, 16, v25
	v_and_b32_e32 v19, 0xffff0000, v25
	s_waitcnt lgkmcnt(7)
	v_pk_mul_f32 v[16:17], v[132:133], v[16:17] op_sel_hi:[0,1]
	v_pk_mul_f32 v[18:19], v[132:133], v[18:19] op_sel_hi:[0,1]
	v_cvt_pk_bf16_f32 v16, v16, v17
	v_cvt_pk_bf16_f32 v17, v18, v19
	v_lshlrev_b32_e32 v18, 16, v26
	v_and_b32_e32 v19, 0xffff0000, v26
	v_lshlrev_b32_e32 v20, 16, v27
	v_and_b32_e32 v21, 0xffff0000, v27
	v_pk_mul_f32 v[18:19], v[132:133], v[18:19] op_sel_hi:[0,1]
	v_pk_mul_f32 v[20:21], v[132:133], v[20:21] op_sel_hi:[0,1]
	v_cvt_pk_bf16_f32 v18, v18, v19
	v_cvt_pk_bf16_f32 v19, v20, v21
	ds_write_b128 v193, v[16:19] offset:18432
	s_waitcnt lgkmcnt(0)
	s_barrier
	ds_read_b128 v[16:19], v169
	ds_read_b64_tr_b16 v[20:21], v170
	ds_read_b64_tr_b16 v[22:23], v170 offset:576
	ds_read_b128 v[32:35], v171
	ds_read_b64_tr_b16 v[36:37], v172
	ds_read_b64_tr_b16 v[38:39], v172 offset:576
	ds_read_b128 v[40:43], v173
	ds_read_b64_tr_b16 v[44:45], v174
	ds_read_b64_tr_b16 v[46:47], v174 offset:576
	ds_read_b128 v[104:107], v175
	ds_read_b64_tr_b16 v[108:109], v176
	ds_read_b64_tr_b16 v[110:111], v176 offset:576
	ds_read_b128 v[194:197], v177
	ds_read_b64_tr_b16 v[198:199], v180
	ds_read_b64_tr_b16 v[200:201], v180 offset:576
	ds_read_b128 v[202:205], v181
	ds_read_b64_tr_b16 v[206:207], v182
	ds_read_b64_tr_b16 v[208:209], v182 offset:576
	ds_read_b128 v[210:213], v183
	ds_read_b64_tr_b16 v[214:215], v184
	ds_read_b64_tr_b16 v[216:217], v184 offset:576
	ds_read_b128 v[218:221], v185
	ds_read_b64_tr_b16 v[222:223], v186
	ds_read_b64_tr_b16 v[224:225], v186 offset:576
	s_waitcnt lgkmcnt(14)
	v_mfma_f32_32x32x16_bf16 v[16:31], v[16:19], v[20:23], 0
	v_mfma_f32_32x32x16_bf16 v[16:31], v[32:35], v[36:39], v[16:31]
	v_mfma_f32_32x32x16_bf16 v[16:31], v[40:43], v[44:47], v[16:31]
	s_waitcnt lgkmcnt(12)
	v_mfma_f32_32x32x16_bf16 v[16:31], v[104:107], v[108:111], v[16:31]
	s_waitcnt lgkmcnt(9)
	v_mfma_f32_32x32x16_bf16 v[16:31], v[194:197], v[198:201], v[16:31]
	ds_read_b128 v[32:35], v187 offset:53248
	ds_read_b128 v[104:107], v187 offset:53280
	ds_read_b128 v[36:39], v188
	ds_read_b128 v[108:111], v188 offset:32
	ds_read_b128 v[194:197], v187 offset:53312
	ds_read_b128 v[198:201], v187 offset:53344
	ds_read_b128 v[226:229], v188 offset:64
	ds_read_b128 v[230:233], v188 offset:96
	s_waitcnt lgkmcnt(14)
	v_mfma_f32_32x32x16_bf16 v[16:31], v[202:205], v[206:209], v[16:31]
	ds_read_b128 v[202:205], v187 offset:53376
	ds_read_b128 v[206:209], v187 offset:53408
	ds_read_b128 v[236:239], v188 offset:128
	ds_read_b128 v[240:243], v188 offset:160
	ds_read_b128 v[244:247], v187 offset:53440
	ds_read_b128 v[248:251], v187 offset:53472
	ds_read_b128 v[134:137], v188 offset:192
	ds_read_b128 v[124:127], v188 offset:224
	s_waitcnt lgkmcnt(14)
; __device__ __forceinline__ unsigned short f2bf(float f) { return (unsigned short)(pk2(f, 0.f) & 0xffffu); }
; __device__ __forceinline__ int accrow(int t, int h) { return (t & 3) + 8 * (t >> 2) + 4 * h; }
; #define MFMA32(a, b, c) __builtin_amdgcn_mfma_f32_32x32x16_bf16((a), (b), (c), 0, 0, 0)
; __device__ __forceinline__ void ssd_unit(const Frame& F, int layer, int unit) {
;     ...
;             for (int ks = 0; ks < 8; ++ks) y = MFMA32(fa[ks], fb[ks], y);
; #pragma unroll
;             for (int ks = 0; ks < 8; ++ks) { fa[ks] = frag_rm(L + SS_CM, 272, 32 * lb, 16 * ks, lane); fb[ks] = frag_rm(L + SS_H, 272, 32 * pb, 16 * ks, lane); }
;             __builtin_amdgcn_sched_barrier(0);
; #pragma unroll
;             for (int ks = 0; ks < 8; ++ks) yo = MFMA32(fa[ks], fb[ks], yo);
;             __builtin_amdgcn_sched_barrier(0);
; #pragma unroll
;             for (int t = 0; t < 16; ++t) { const int l = 32 * lb + accrow(t, lane >> 5); Yout[(size_t)(row0 + l) * 512 + hd * 64 + 32 * pb + (lane & 31)] = f2bf(y[t] + erow[l] * yo[t]); }
	v_mfma_f32_32x32x16_bf16 v[16:31], v[210:213], v[214:217], v[16:31]
	s_waitcnt lgkmcnt(13)
	v_mfma_f32_32x32x16_bf16 v[32:47], v[32:35], v[36:39], 0
	s_waitcnt lgkmcnt(12)
	v_mfma_f32_32x32x16_bf16 v[32:47], v[104:107], v[108:111], v[32:47]
	s_waitcnt lgkmcnt(9)
	v_mfma_f32_32x32x16_bf16 v[32:47], v[194:197], v[226:229], v[32:47]
	s_waitcnt lgkmcnt(8)
	v_mfma_f32_32x32x16_bf16 v[32:47], v[198:201], v[230:233], v[32:47]
	s_waitcnt lgkmcnt(5)
	v_mfma_f32_32x32x16_bf16 v[32:47], v[202:205], v[236:239], v[32:47]
	s_waitcnt lgkmcnt(4)
	v_mfma_f32_32x32x16_bf16 v[32:47], v[206:209], v[240:243], v[32:47]
	s_waitcnt lgkmcnt(1)
	v_mfma_f32_32x32x16_bf16 v[32:47], v[244:247], v[134:137], v[32:47]
	s_waitcnt lgkmcnt(0)
	v_mfma_f32_32x32x16_bf16 v[32:47], v[248:251], v[124:127], v[32:47]
	v_mfma_f32_32x32x16_bf16 v[16:31], v[218:221], v[222:225], v[16:31]
	v_lshl_add_u32 v104, v156, 2, s26
	ds_read_b128 v[104:107], v104
	v_lshl_add_u32 v108, v157, 2, s26
	ds_read_b128 v[108:111], v108
	ds_read_b128 v[194:197], v160
	ds_read_b128 v[198:201], v165
	v_mbcnt_lo_u32_b32 v202, -1, 0
	v_mbcnt_hi_u32_b32 v202, -1, v202
	v_readlane_b32 s5, v254, 6
	s_nop 3
	s_mul_i32 s5, s5, 1280
	s_add_i32 s5, s5, 142400
	v_and_b32_e32 v203, 31, v202
	v_lshrrev_b32_e32 v204, 5, v202
	v_mul_u32_u24_e32 v204, 320, v204
	v_lshl_add_u32 v204, v203, 1, v204
	v_add_u32_e32 v204, s5, v204
	v_lshrrev_b32_e32 v205, 2, v202
	v_and_b32_e32 v206, 3, v202
	v_mul_u32_u24_e32 v207, 80, v205
	v_lshl_add_u32 v207, v206, 4, v207
	v_add_u32_e32 v207, s5, v207
	v_and_b32_e32 v208, 0xffffffe0, v156
	v_add3_u32 v208, v208, v205, s4
	v_ashrrev_i32_e32 v209, 31, v208
	v_lshlrev_b64 v[208:209], 10, v[208:209]
	v_lshlrev_b32_e32 v210, 4, v206
	v_lshlrev_b32_e32 v211, 1, v203
	v_sub_u32_e32 v210, v210, v211
	v_ashrrev_i32_e32 v211, 31, v210
	v_lshl_add_u64 v[208:209], v[128:129], 0, v[208:209]
	v_lshl_add_u64 v[208:209], v[208:209], 0, v[210:211]
	v_mov_b32_e32 v220, 0x4000
	v_mov_b32_e32 v221, 0
	s_waitcnt lgkmcnt(0)
	s_nop 7
	v_fma_f32 v16, v32, v104, v16
	v_fma_f32 v17, v33, v105, v17
	v_fma_f32 v18, v34, v106, v18
	v_fma_f32 v19, v35, v107, v19
	v_fma_f32 v20, v36, v108, v20
	v_fma_f32 v21, v37, v109, v21
	v_fma_f32 v22, v38, v110, v22
	v_fma_f32 v23, v39, v111, v23
	v_fma_f32 v24, v40, v194, v24
	v_fma_f32 v25, v41, v195, v25
	v_fma_f32 v26, v42, v196, v26
	v_fma_f32 v27, v43, v197, v27
	v_fma_f32 v28, v44, v198, v28
	v_fma_f32 v29, v45, v199, v29
	v_fma_f32 v30, v46, v200, v30
	v_fma_f32 v31, v47, v201, v31
	v_cvt_pk_bf16_f32 v16, v16, v16
	v_cvt_pk_bf16_f32 v17, v17, v17
	v_cvt_pk_bf16_f32 v18, v18, v18
	v_cvt_pk_bf16_f32 v19, v19, v19
	v_cvt_pk_bf16_f32 v20, v20, v20
	v_cvt_pk_bf16_f32 v21, v21, v21
	v_cvt_pk_bf16_f32 v22, v22, v22
	v_cvt_pk_bf16_f32 v23, v23, v23
	v_cvt_pk_bf16_f32 v24, v24, v24
	v_cvt_pk_bf16_f32 v25, v25, v25
	v_cvt_pk_bf16_f32 v26, v26, v26
	v_cvt_pk_bf16_f32 v27, v27, v27
	v_cvt_pk_bf16_f32 v28, v28, v28
	v_cvt_pk_bf16_f32 v29, v29, v29
	v_cvt_pk_bf16_f32 v30, v30, v30
	v_cvt_pk_bf16_f32 v31, v31, v31
	ds_write_b16 v204, v16 offset:0
	ds_write_b16 v204, v17 offset:80
	ds_write_b16 v204, v18 offset:160
	ds_write_b16 v204, v19 offset:240
	ds_write_b16 v204, v20 offset:640
	ds_write_b16 v204, v21 offset:720
	ds_write_b16 v204, v22 offset:800
	ds_write_b16 v204, v23 offset:880
	s_waitcnt lgkmcnt(0)
	ds_read_b128 v[212:215], v207
	s_waitcnt lgkmcnt(0)
	global_store_dwordx4 v[208:209], v[212:215], off
	v_lshl_add_u64 v[208:209], v[208:209], 0, v[220:221]
	ds_write_b16 v204, v24 offset:0
	ds_write_b16 v204, v25 offset:80
	ds_write_b16 v204, v26 offset:160
	ds_write_b16 v204, v27 offset:240
	ds_write_b16 v204, v28 offset:640
	ds_write_b16 v204, v29 offset:720
	ds_write_b16 v204, v30 offset:800
	ds_write_b16 v204, v31 offset:880
	s_waitcnt lgkmcnt(0)
	ds_read_b128 v[216:219], v207
	s_waitcnt lgkmcnt(0)
	global_store_dwordx4 v[208:209], v[216:219], off
	s_waitcnt lgkmcnt(0)
	s_barrier
; #define LAS __attribute__((address_space(3)))
; __device__ __forceinline__ unsigned short f2bf(float f) { return (unsigned short)(pk2(f, 0.f) & 0xffffu); }
; __device__ __forceinline__ void lds_barrier() { asm volatile("s_waitcnt lgkmcnt(0)" ::: "memory"); __builtin_amdgcn_s_barrier(); asm volatile("" ::: "memory"); }
; __device__ __forceinline__ int accrow(int t, int h) { return (t & 3) + 8 * (t >> 2) + 4 * h; }
; #define MFMA32(a, b, c) __builtin_amdgcn_mfma_f32_32x32x16_bf16((a), (b), (c), 0, 0, 0)
; __device__ __forceinline__ void ssd_unit(const Frame& F, int layer, int unit) {
;     ...
;         {
;             const int pb = wave & 1, nb = wave >> 1; const float dec = aendp[0];
;             bf16x8 fa[8], fb[8];
; #pragma unroll
;             for (int ks = 0; ks < 8; ++ks) { fa[ks] = frag_tr(L + SS_XS, SS_XS_STRIDE, 16 * ks, 32 * pb, lane); fb[ks] = frag_tr(L + SS_BM, 272, 16 * ks, 32 * nb, lane); }
; #pragma unroll
;             for (int t = 0; t < 16; ++t) hacc[t] *= dec;
;             __builtin_amdgcn_sched_barrier(0);
; #pragma unroll
;             for (int ks = 0; ks < 8; ++ks) hacc = MFMA32(fa[ks], fb[ks], hacc);
; #pragma unroll
;             for (int t = 0; t < 16; ++t) *(LAS bf16_t*)(L + SS_H + (32 * pb + accrow(t, lane >> 5)) * 272 + (32 * nb + (lane & 31)) * 2) = f2bf(hacc[t]);
;         }
;         lds_barrier();
;         if (step + 1 < 18) SS_STORE();
	v_mov_b32_e32 v16, s27
	ds_read_b32 v132, v16
	ds_read_b64_tr_b16 v[16:17], v170
	ds_read_b64_tr_b16 v[20:21], v189 offset:35840
	ds_read_b64_tr_b16 v[18:19], v170 offset:576
	ds_read_b64_tr_b16 v[26:27], v189 offset:19520
	ds_read_b64_tr_b16 v[28:29], v189 offset:22784
	ds_read_b64_tr_b16 v[30:31], v189 offset:23872
	ds_read_b64_tr_b16 v[32:33], v189 offset:27136
	ds_read_b64_tr_b16 v[38:39], v190 offset:576
	ds_read_b64_tr_b16 v[40:41], v190 offset:2304
	ds_read_b64_tr_b16 v[42:43], v190 offset:2880
	ds_read_b64_tr_b16 v[44:45], v190 offset:4608
	ds_read_b64_tr_b16 v[36:37], v190
	ds_read_b64_tr_b16 v[34:35], v189 offset:28224
	ds_read_b64_tr_b16 v[104:105], v189 offset:31488
	ds_read_b64_tr_b16 v[106:107], v189 offset:32576
	ds_read_b64_tr_b16 v[46:47], v190 offset:5184
	ds_read_b64_tr_b16 v[108:109], v190 offset:6912
	ds_read_b64_tr_b16 v[110:111], v190 offset:7488
	ds_read_b64_tr_b16 v[124:125], v190 offset:9216
	ds_read_b64_tr_b16 v[22:23], v189 offset:36928
	ds_read_b64_tr_b16 v[134:135], v189 offset:40192
	ds_read_b64_tr_b16 v[136:137], v189 offset:41280
	ds_read_b64_tr_b16 v[194:195], v189 offset:44544
	ds_read_b64_tr_b16 v[126:127], v190 offset:9792
	ds_read_b64_tr_b16 v[198:199], v190 offset:11520
	ds_read_b64_tr_b16 v[200:201], v190 offset:12096
	ds_read_b64_tr_b16 v[202:203], v190 offset:13824
	ds_read_b64_tr_b16 v[204:205], v190 offset:14400
	ds_read_b64_tr_b16 v[24:25], v189 offset:18432
	ds_read_b64_tr_b16 v[196:197], v189 offset:45632
	ds_read_b64_tr_b16 v[206:207], v189 offset:48896
	ds_read_b64_tr_b16 v[208:209], v189 offset:49984
	s_waitcnt lgkmcnt(14)
	v_pk_mul_f32 v[14:15], v[14:15], v[132:133] op_sel_hi:[1,0]
	v_pk_mul_f32 v[12:13], v[12:13], v[132:133] op_sel_hi:[1,0]
	v_pk_mul_f32 v[10:11], v[10:11], v[132:133] op_sel_hi:[1,0]
	v_pk_mul_f32 v[8:9], v[8:9], v[132:133] op_sel_hi:[1,0]
	v_pk_mul_f32 v[6:7], v[6:7], v[132:133] op_sel_hi:[1,0]
	v_pk_mul_f32 v[4:5], v[4:5], v[132:133] op_sel_hi:[1,0]
	v_pk_mul_f32 v[2:3], v[2:3], v[132:133] op_sel_hi:[1,0]
	v_pk_mul_f32 v[0:1], v[0:1], v[132:133] op_sel_hi:[1,0]
	s_waitcnt lgkmcnt(3)
	s_nop 0
	v_mfma_f32_32x32x16_bf16 v[0:15], v[16:19], v[24:27], v[0:15]
	s_andn2_b64 vcc, exec, s[2:3]
	v_mfma_f32_32x32x16_bf16 v[0:15], v[36:39], v[28:31], v[0:15]
	v_mfma_f32_32x32x16_bf16 v[0:15], v[40:43], v[32:35], v[0:15]
	v_mfma_f32_32x32x16_bf16 v[0:15], v[44:47], v[104:107], v[0:15]
	v_mfma_f32_32x32x16_bf16 v[0:15], v[108:111], v[20:23], v[0:15]
	v_mfma_f32_32x32x16_bf16 v[0:15], v[124:127], v[134:137], v[0:15]
	s_waitcnt lgkmcnt(2)
	v_mfma_f32_32x32x16_bf16 v[0:15], v[198:201], v[194:197], v[0:15]
	s_waitcnt lgkmcnt(0)
	v_mfma_f32_32x32x16_bf16 v[0:15], v[202:205], v[206:209], v[0:15]
	s_nop 11
	v_cvt_pk_bf16_f32 v16, v0, s0
	v_cvt_pk_bf16_f32 v17, v1, s0
	v_cvt_pk_bf16_f32 v18, v2, s0
	v_cvt_pk_bf16_f32 v19, v3, s0
	v_cvt_pk_bf16_f32 v20, v4, s0
	v_cvt_pk_bf16_f32 v21, v5, s0
	v_cvt_pk_bf16_f32 v22, v6, s0
	v_cvt_pk_bf16_f32 v23, v7, s0
	v_cvt_pk_bf16_f32 v24, v8, s0
	v_cvt_pk_bf16_f32 v25, v9, s0
	v_cvt_pk_bf16_f32 v26, v10, s0
	v_cvt_pk_bf16_f32 v27, v11, s0
	v_cvt_pk_bf16_f32 v28, v12, s0
	v_cvt_pk_bf16_f32 v29, v13, s0
	v_cvt_pk_bf16_f32 v30, v14, s0
	v_cvt_pk_bf16_f32 v31, v15, s0
	ds_write_b16 v191, v16
	ds_write_b16 v191, v17 offset:272
	ds_write_b16 v191, v18 offset:544
	ds_write_b16 v191, v19 offset:816
	ds_write_b16 v191, v20 offset:2176
	ds_write_b16 v191, v21 offset:2448
	ds_write_b16 v191, v22 offset:2720
	ds_write_b16 v191, v23 offset:2992
	ds_write_b16 v191, v24 offset:4352
	ds_write_b16 v191, v25 offset:4624
	ds_write_b16 v191, v26 offset:4896
	ds_write_b16 v191, v27 offset:5168
	ds_write_b16 v191, v28 offset:6528
	ds_write_b16 v191, v29 offset:6800
	ds_write_b16 v191, v30 offset:7072
	ds_write_b16 v191, v31 offset:7344
	s_waitcnt lgkmcnt(0)
	s_barrier
	s_cbranch_vccnz .LBB0_653
	s_waitcnt vmcnt(15)
	ds_write_b128 v146, v[48:51]
	s_waitcnt vmcnt(14)
	ds_write_b128 v147, v[52:55]
	s_waitcnt vmcnt(13)
	ds_write_b128 v148, v[56:59] offset:18432
	s_waitcnt vmcnt(12)
	ds_write_b128 v148, v[60:63] offset:53248
	s_waitcnt vmcnt(11)
	ds_write_b128 v149, v[64:67]
	s_waitcnt vmcnt(10)
	ds_write_b128 v150, v[68:71] offset:18432
	s_waitcnt vmcnt(9)
	ds_write_b128 v150, v[72:75] offset:53248
	s_waitcnt vmcnt(8)
	ds_write_b128 v151, v[76:79]
	s_waitcnt vmcnt(7)
	ds_write_b128 v152, v[80:83] offset:18432
	s_waitcnt vmcnt(6)
	ds_write_b128 v152, v[84:87] offset:53248
	s_waitcnt vmcnt(5)
	ds_write_b128 v153, v[88:91]
	s_waitcnt vmcnt(4)
	ds_write_b128 v154, v[92:95] offset:18432
	s_waitcnt vmcnt(3)
	ds_write_b128 v154, v[96:99] offset:53248
	s_waitcnt vmcnt(2)
	ds_write_b128 v155, v[100:103]
	s_branch .LBB0_653
